# baseline (speedup 1.0000x reference)
.LBB1_4:
	s_or_b64 exec, exec, s[4:5]
	v_cmp_eq_u32_e64 s[4:5], 0, v0
	s_and_saveexec_b64 s[6:7], s[4:5]
	v_mov_b32_e32 v1, 0
	v_mov_b32_e32 v2, 0x10408
	ds_write_b32 v2, v1
	s_or_b64 exec, exec, s[6:7]
	v_cmp_gt_u32_e64 s[6:7], 64, v0
	v_mbcnt_lo_u32_b32 v1, -1, 0
	s_waitcnt lgkmcnt(0)
	s_barrier
	s_and_saveexec_b64 s[8:9], s[6:7]
	s_cbranch_execz .LBB1_9
	v_mov_b32_e32 v2, 0x10410
	v_lshl_add_u32 v3, v0, 4, v2
	ds_read_b128 v[8:11], v3
	s_waitcnt lgkmcnt(0)
	v_add_u32_e32 v7, v9, v8
	v_add3_u32 v7, v7, v10, v11
	v_mov_b32_e32 v2, v7
	s_nop 1
	v_add_u32_dpp v2, v2, v2 row_shr:1 row_mask:0xf bank_mask:0xf
	s_nop 1
	v_add_u32_dpp v2, v2, v2 row_shr:2 row_mask:0xf bank_mask:0xf
	s_nop 1
	v_add_u32_dpp v2, v2, v2 row_shr:4 row_mask:0xf bank_mask:0xf
	s_nop 1
	v_add_u32_dpp v2, v2, v2 row_shr:8 row_mask:0xf bank_mask:0xf
	s_nop 1
	v_add_u32_dpp v2, v2, v2 row_bcast:15 row_mask:0xa bank_mask:0xf
	s_nop 1
	v_add_u32_dpp v2, v2, v2 row_bcast:31 row_mask:0xc bank_mask:0xf
	v_sub_u32_e32 v12, v2, v7
	v_add_u32_e32 v13, v12, v8
	v_add_u32_e32 v14, v13, v9
	v_add_u32_e32 v15, v14, v10
	v_cmp_eq_u32_e32 vcc, 63, v0
	ds_write_b128 v3, v[12:15]
	s_and_b64 exec, exec, vcc
	v_mov_b32_e32 v3, 0x10810
	ds_write_b32 v3, v2

.LBB1_41:
	s_load_dwordx8 s[16:23], s[0:1], 0x18
	s_load_dwordx2 s[8:9], s[0:1], 0x38
	v_cmp_lt_i32_e32 vcc, s3, v77
	s_waitcnt lgkmcnt(0)
	s_barrier
	s_and_saveexec_b64 s[10:11], s[6:7]
	s_cbranch_execz .LBB1_44
	v_lshlrev_b32_e32 v13, 4, v0
	v_add_u32_e32 v7, 0x10820, v13
	ds_read_b128 v[8:11], v7
	s_waitcnt lgkmcnt(0)
	v_add_u32_e32 v15, v9, v8
	v_add3_u32 v11, v15, v10, v11
	v_mov_b32_e32 v7, v11
	s_nop 1
	v_add_u32_dpp v7, v7, v7 row_shr:1 row_mask:0xf bank_mask:0xf
	s_nop 1
	v_add_u32_dpp v7, v7, v7 row_shr:2 row_mask:0xf bank_mask:0xf
	s_nop 1
	v_add_u32_dpp v7, v7, v7 row_shr:4 row_mask:0xf bank_mask:0xf
	s_nop 1
	v_add_u32_dpp v7, v7, v7 row_shr:8 row_mask:0xf bank_mask:0xf
	s_nop 1
	v_add_u32_dpp v7, v7, v7 row_bcast:15 row_mask:0xa bank_mask:0xf
	s_nop 1
	v_add_u32_dpp v7, v7, v7 row_bcast:31 row_mask:0xc bank_mask:0xf
	v_sub_u32_e32 v12, v7, v11
	v_or_b32_e32 v11, 0x10000, v13
	v_add_u32_e32 v13, v12, v8
	v_add_u32_e32 v14, v13, v9
	v_add_u32_e32 v15, v14, v10
	v_cmp_eq_u32_e64 s[0:1], 63, v0
	ds_write_b128 v11, v[12:15]
	s_and_b64 exec, exec, s[0:1]
	v_mov_b32_e32 v8, 0x10400
	ds_write_b32 v8, v7
